# attention epilogue: 64 byte stores per lane replaced by 16 dword stores (4x4 byte transpose inside each lane quad with DPP quad_perm + v_perm), same per-element math
# baseline (speedup 1.0000x reference)
; __device__ __forceinline__ int crow(int r, int hi) { return (r & 3) + 8 * (r >> 2) + 4 * hi; }
; __device__ __forceinline__ void attn_unit(const bf16* __restrict__ Qlane, const bf16* __restrict__ Kh, const bf16* __restrict__ Vh, unsigned char* __restrict__ Ow, int ldo, ...
;     ...
;   if (hi == 0) li_l[r32] = l_reg; asm volatile("s_waitcnt lgkmcnt(0)" ::: "memory");
;   float rli[16];
; #pragma unroll
;   for (int r = 0; r < 16; ++r) rli[r] = __builtin_amdgcn_rcpf(li_l[crow(r, hi)]);
;   unsigned ob = (unsigned)(4 * hi * ldo + r32); asm volatile("" : "+v"(ob));
; #pragma unroll
;   for (int r = 0; r < 16; ++r) { const int orow0 = crow(r, 0);
; #pragma unroll
;     for (int d0 = 0; d0 < 4; ++d0) Ow[ob + (unsigned)(orow0 * ldo + d0 * 32)] = (unsigned char)(__builtin_amdgcn_cvt_pk_fp8_f32(__builtin_amdgcn_fmed3f(o[d0][r] * rli[r] * F8_MSCALE, -448.f, 448.f), 0.f, 0, false) & 0xff); }
.LBB0_777:
	s_or_b64 exec, exec, s[2:3]
	s_waitcnt lgkmcnt(0)
	ds_read_b128 v[74:77], v203
	ds_read_b128 v[78:81], v203 offset:32
	s_or_b32 s2, s56, s44
	s_lshl_b32 s2, s2, 11
	s_add_u32 s2, s41, s2
	s_addc_u32 s3, s42, 0
	s_add_u32 s2, s2, s8
	s_addc_u32 s3, s3, 0
	s_mov_b32 s98, 0x5040100
	v_and_b32_e32 v66, 3, v178
	v_and_b32_e32 v67, 28, v178
	v_lshrrev_b32_e32 v68, 5, v178
	v_add_u32_e32 v1, 4, v66
	v_lshl_add_u32 v82, v66, 5, v67
	v_lshl_or_b32 v1, v1, 8, v66
	v_lshl_or_b32 v82, v68, 13, v82
	v_or_b32_e32 v1, 0xc0c0000, v1
	s_waitcnt lgkmcnt(0)
	v_rcp_f32_e32 v74, v74
	v_rcp_f32_e32 v75, v75
	v_rcp_f32_e32 v76, v76
	v_rcp_f32_e32 v77, v77
	v_rcp_f32_e32 v78, v78
	v_rcp_f32_e32 v79, v79
	v_rcp_f32_e32 v80, v80
	v_rcp_f32_e32 v81, v81
	v_mul_f32_e32 v50, v50, v74
	v_mul_f32_e32 v34, v34, v74
	v_mul_f32_e32 v18, v18, v74
	v_mul_f32_e32 v2, v2, v74
	v_mul_f32_e32 v50, 0x41800000, v50
	v_mul_f32_e32 v34, 0x41800000, v34
	v_mul_f32_e32 v18, 0x41800000, v18
	v_mul_f32_e32 v2, 0x41800000, v2
	v_med3_f32 v50, v50, s54, v221
	v_med3_f32 v34, v34, s54, v221
	v_med3_f32 v18, v18, s54, v221
	v_med3_f32 v2, v2, s54, v221
	v_cvt_pk_fp8_f32 v66, v50, v34
	v_cvt_pk_fp8_f32 v66, v18, v2 op_sel:[0,0,1]
	s_nop 1
	v_mov_b32_dpp v50, v66 quad_perm:[0,0,0,0] row_mask:0xf bank_mask:0xf
	v_mov_b32_dpp v34, v66 quad_perm:[1,1,1,1] row_mask:0xf bank_mask:0xf
	v_mov_b32_dpp v18, v66 quad_perm:[2,2,2,2] row_mask:0xf bank_mask:0xf
	v_mov_b32_dpp v2, v66 quad_perm:[3,3,3,3] row_mask:0xf bank_mask:0xf
	v_perm_b32 v67, v34, v50, v1
	v_perm_b32 v68, v2, v18, v1
	v_perm_b32 v69, v68, v67, s98
	global_store_dword v82, v69, s[2:3]
	v_mul_f32_e32 v51, v51, v75
	v_mul_f32_e32 v35, v35, v75
	v_mul_f32_e32 v19, v19, v75
	v_mul_f32_e32 v3, v3, v75
	v_mul_f32_e32 v51, 0x41800000, v51
	v_mul_f32_e32 v35, 0x41800000, v35
	v_mul_f32_e32 v19, 0x41800000, v19
	v_mul_f32_e32 v3, 0x41800000, v3
	v_med3_f32 v51, v51, s54, v221
	v_med3_f32 v35, v35, s54, v221
	v_med3_f32 v19, v19, s54, v221
	v_med3_f32 v3, v3, s54, v221
	v_cvt_pk_fp8_f32 v71, v51, v35
	v_cvt_pk_fp8_f32 v71, v19, v3 op_sel:[0,0,1]
	s_nop 1
	v_mov_b32_dpp v51, v71 quad_perm:[0,0,0,0] row_mask:0xf bank_mask:0xf
	v_mov_b32_dpp v35, v71 quad_perm:[1,1,1,1] row_mask:0xf bank_mask:0xf
	v_mov_b32_dpp v19, v71 quad_perm:[2,2,2,2] row_mask:0xf bank_mask:0xf
	v_mov_b32_dpp v3, v71 quad_perm:[3,3,3,3] row_mask:0xf bank_mask:0xf
	v_perm_b32 v72, v35, v51, v1
	v_perm_b32 v73, v3, v19, v1
	v_perm_b32 v69, v73, v72, s98
	v_add_u32_e32 v70, 0x800, v82
	global_store_dword v70, v69, s[2:3]
	v_mul_f32_e32 v52, v52, v76
	v_mul_f32_e32 v36, v36, v76
	v_mul_f32_e32 v20, v20, v76
	v_mul_f32_e32 v4, v4, v76
	v_mul_f32_e32 v52, 0x41800000, v52
	v_mul_f32_e32 v36, 0x41800000, v36
	v_mul_f32_e32 v20, 0x41800000, v20
	v_mul_f32_e32 v4, 0x41800000, v4
	v_med3_f32 v52, v52, s54, v221
	v_med3_f32 v36, v36, s54, v221
	v_med3_f32 v20, v20, s54, v221
	v_med3_f32 v4, v4, s54, v221
	v_cvt_pk_fp8_f32 v66, v52, v36
	v_cvt_pk_fp8_f32 v66, v20, v4 op_sel:[0,0,1]
	s_nop 1
	v_mov_b32_dpp v52, v66 quad_perm:[0,0,0,0] row_mask:0xf bank_mask:0xf
	v_mov_b32_dpp v36, v66 quad_perm:[1,1,1,1] row_mask:0xf bank_mask:0xf
	v_mov_b32_dpp v20, v66 quad_perm:[2,2,2,2] row_mask:0xf bank_mask:0xf
	v_mov_b32_dpp v4, v66 quad_perm:[3,3,3,3] row_mask:0xf bank_mask:0xf
	v_perm_b32 v67, v36, v52, v1
	v_perm_b32 v68, v4, v20, v1
	v_perm_b32 v69, v68, v67, s98
	v_add_u32_e32 v70, 0x1000, v82
	global_store_dword v70, v69, s[2:3]
	v_mul_f32_e32 v53, v53, v77
	v_mul_f32_e32 v37, v37, v77
	v_mul_f32_e32 v21, v21, v77
	v_mul_f32_e32 v5, v5, v77
	v_mul_f32_e32 v53, 0x41800000, v53
	v_mul_f32_e32 v37, 0x41800000, v37
	v_mul_f32_e32 v21, 0x41800000, v21
	v_mul_f32_e32 v5, 0x41800000, v5
	v_med3_f32 v53, v53, s54, v221
	v_med3_f32 v37, v37, s54, v221
	v_med3_f32 v21, v21, s54, v221
	v_med3_f32 v5, v5, s54, v221
	v_cvt_pk_fp8_f32 v71, v53, v37
	v_cvt_pk_fp8_f32 v71, v21, v5 op_sel:[0,0,1]
	s_nop 1
	v_mov_b32_dpp v53, v71 quad_perm:[0,0,0,0] row_mask:0xf bank_mask:0xf
	v_mov_b32_dpp v37, v71 quad_perm:[1,1,1,1] row_mask:0xf bank_mask:0xf
	v_mov_b32_dpp v21, v71 quad_perm:[2,2,2,2] row_mask:0xf bank_mask:0xf
	v_mov_b32_dpp v5, v71 quad_perm:[3,3,3,3] row_mask:0xf bank_mask:0xf
	v_perm_b32 v72, v37, v53, v1
	v_perm_b32 v73, v5, v21, v1
	v_perm_b32 v69, v73, v72, s98
	v_add_u32_e32 v70, 0x1800, v82
	global_store_dword v70, v69, s[2:3]
	v_mul_f32_e32 v54, v54, v78
	v_mul_f32_e32 v38, v38, v78
	v_mul_f32_e32 v22, v22, v78
	v_mul_f32_e32 v6, v6, v78
	v_mul_f32_e32 v54, 0x41800000, v54
	v_mul_f32_e32 v38, 0x41800000, v38
	v_mul_f32_e32 v22, 0x41800000, v22
	v_mul_f32_e32 v6, 0x41800000, v6
	v_med3_f32 v54, v54, s54, v221
	v_med3_f32 v38, v38, s54, v221
	v_med3_f32 v22, v22, s54, v221
	v_med3_f32 v6, v6, s54, v221
	v_cvt_pk_fp8_f32 v66, v54, v38
	v_cvt_pk_fp8_f32 v66, v22, v6 op_sel:[0,0,1]
	s_nop 1
	v_mov_b32_dpp v54, v66 quad_perm:[0,0,0,0] row_mask:0xf bank_mask:0xf
	v_mov_b32_dpp v38, v66 quad_perm:[1,1,1,1] row_mask:0xf bank_mask:0xf
	v_mov_b32_dpp v22, v66 quad_perm:[2,2,2,2] row_mask:0xf bank_mask:0xf
	v_mov_b32_dpp v6, v66 quad_perm:[3,3,3,3] row_mask:0xf bank_mask:0xf
	v_perm_b32 v67, v38, v54, v1
	v_perm_b32 v68, v6, v22, v1
	v_perm_b32 v69, v68, v67, s98
	v_add_u32_e32 v70, 0x4000, v82
	global_store_dword v70, v69, s[2:3]
	v_mul_f32_e32 v55, v55, v79
	v_mul_f32_e32 v39, v39, v79
	v_mul_f32_e32 v23, v23, v79
	v_mul_f32_e32 v7, v7, v79
	v_mul_f32_e32 v55, 0x41800000, v55
	v_mul_f32_e32 v39, 0x41800000, v39
	v_mul_f32_e32 v23, 0x41800000, v23
	v_mul_f32_e32 v7, 0x41800000, v7
	v_med3_f32 v55, v55, s54, v221
	v_med3_f32 v39, v39, s54, v221
	v_med3_f32 v23, v23, s54, v221
	v_med3_f32 v7, v7, s54, v221
; __device__ __forceinline__ int crow(int r, int hi) { return (r & 3) + 8 * (r >> 2) + 4 * hi; }
; __device__ __forceinline__ void attn_unit(const bf16* __restrict__ Qlane, const bf16* __restrict__ Kh, const bf16* __restrict__ Vh, unsigned char* __restrict__ Ow, int ldo, ...
;     ...
;   for (int r = 0; r < 16; ++r) rli[r] = __builtin_amdgcn_rcpf(li_l[crow(r, hi)]);
;   unsigned ob = (unsigned)(4 * hi * ldo + r32); asm volatile("" : "+v"(ob));
; #pragma unroll
;   for (int r = 0; r < 16; ++r) { const int orow0 = crow(r, 0);
; #pragma unroll
;     for (int d0 = 0; d0 < 4; ++d0) Ow[ob + (unsigned)(orow0 * ldo + d0 * 32)] = (unsigned char)(__builtin_amdgcn_cvt_pk_fp8_f32(__builtin_amdgcn_fmed3f(o[d0][r] * rli[r] * F8_MSCALE, -448.f, 448.f), 0.f, 0, false) & 0xff); }
	v_cvt_pk_fp8_f32 v71, v55, v39
	v_cvt_pk_fp8_f32 v71, v23, v7 op_sel:[0,0,1]
	s_nop 1
	v_mov_b32_dpp v55, v71 quad_perm:[0,0,0,0] row_mask:0xf bank_mask:0xf
	v_mov_b32_dpp v39, v71 quad_perm:[1,1,1,1] row_mask:0xf bank_mask:0xf
	v_mov_b32_dpp v23, v71 quad_perm:[2,2,2,2] row_mask:0xf bank_mask:0xf
	v_mov_b32_dpp v7, v71 quad_perm:[3,3,3,3] row_mask:0xf bank_mask:0xf
	v_perm_b32 v72, v39, v55, v1
	v_perm_b32 v73, v7, v23, v1
	v_perm_b32 v69, v73, v72, s98
	v_add_u32_e32 v70, 0x4800, v82
	global_store_dword v70, v69, s[2:3]
	v_mul_f32_e32 v56, v56, v80
	v_mul_f32_e32 v40, v40, v80
	v_mul_f32_e32 v24, v24, v80
	v_mul_f32_e32 v8, v8, v80
	v_mul_f32_e32 v56, 0x41800000, v56
	v_mul_f32_e32 v40, 0x41800000, v40
	v_mul_f32_e32 v24, 0x41800000, v24
	v_mul_f32_e32 v8, 0x41800000, v8
	v_med3_f32 v56, v56, s54, v221
	v_med3_f32 v40, v40, s54, v221
	v_med3_f32 v24, v24, s54, v221
	v_med3_f32 v8, v8, s54, v221
	v_cvt_pk_fp8_f32 v66, v56, v40
	v_cvt_pk_fp8_f32 v66, v24, v8 op_sel:[0,0,1]
	s_nop 1
	v_mov_b32_dpp v56, v66 quad_perm:[0,0,0,0] row_mask:0xf bank_mask:0xf
	v_mov_b32_dpp v40, v66 quad_perm:[1,1,1,1] row_mask:0xf bank_mask:0xf
	v_mov_b32_dpp v24, v66 quad_perm:[2,2,2,2] row_mask:0xf bank_mask:0xf
	v_mov_b32_dpp v8, v66 quad_perm:[3,3,3,3] row_mask:0xf bank_mask:0xf
	v_perm_b32 v67, v40, v56, v1
	v_perm_b32 v68, v8, v24, v1
	v_perm_b32 v69, v68, v67, s98
	v_add_u32_e32 v70, 0x5000, v82
	global_store_dword v70, v69, s[2:3]
	v_mul_f32_e32 v57, v57, v81
	v_mul_f32_e32 v41, v41, v81
	v_mul_f32_e32 v25, v25, v81
	v_mul_f32_e32 v9, v9, v81
	v_mul_f32_e32 v57, 0x41800000, v57
	v_mul_f32_e32 v41, 0x41800000, v41
	v_mul_f32_e32 v25, 0x41800000, v25
	v_mul_f32_e32 v9, 0x41800000, v9
	v_med3_f32 v57, v57, s54, v221
	v_med3_f32 v41, v41, s54, v221
	v_med3_f32 v25, v25, s54, v221
	v_med3_f32 v9, v9, s54, v221
	v_cvt_pk_fp8_f32 v71, v57, v41
	v_cvt_pk_fp8_f32 v71, v25, v9 op_sel:[0,0,1]
	s_nop 1
	v_mov_b32_dpp v57, v71 quad_perm:[0,0,0,0] row_mask:0xf bank_mask:0xf
	v_mov_b32_dpp v41, v71 quad_perm:[1,1,1,1] row_mask:0xf bank_mask:0xf
	v_mov_b32_dpp v25, v71 quad_perm:[2,2,2,2] row_mask:0xf bank_mask:0xf
	v_mov_b32_dpp v9, v71 quad_perm:[3,3,3,3] row_mask:0xf bank_mask:0xf
	v_perm_b32 v72, v41, v57, v1
	v_perm_b32 v73, v9, v25, v1
	v_perm_b32 v69, v73, v72, s98
	v_add_u32_e32 v70, 0x5800, v82
	global_store_dword v70, v69, s[2:3]
	ds_read_b128 v[74:77], v203 offset:64
	ds_read_b128 v[78:81], v203 offset:96
	s_waitcnt lgkmcnt(0)
	v_rcp_f32_e32 v74, v74
	v_rcp_f32_e32 v75, v75
	v_rcp_f32_e32 v76, v76
	v_rcp_f32_e32 v77, v77
	v_rcp_f32_e32 v78, v78
	v_rcp_f32_e32 v79, v79
	v_rcp_f32_e32 v80, v80
	v_rcp_f32_e32 v81, v81
	v_mul_f32_e32 v58, v58, v74
	v_mul_f32_e32 v42, v42, v74
	v_mul_f32_e32 v26, v26, v74
	v_mul_f32_e32 v10, v10, v74
	v_mul_f32_e32 v58, 0x41800000, v58
	v_mul_f32_e32 v42, 0x41800000, v42
	v_mul_f32_e32 v26, 0x41800000, v26
	v_mul_f32_e32 v10, 0x41800000, v10
	v_med3_f32 v58, v58, s54, v221
	v_med3_f32 v42, v42, s54, v221
	v_med3_f32 v26, v26, s54, v221
	v_med3_f32 v10, v10, s54, v221
	v_cvt_pk_fp8_f32 v66, v58, v42
	v_cvt_pk_fp8_f32 v66, v26, v10 op_sel:[0,0,1]
	s_nop 1
	v_mov_b32_dpp v58, v66 quad_perm:[0,0,0,0] row_mask:0xf bank_mask:0xf
	v_mov_b32_dpp v42, v66 quad_perm:[1,1,1,1] row_mask:0xf bank_mask:0xf
	v_mov_b32_dpp v26, v66 quad_perm:[2,2,2,2] row_mask:0xf bank_mask:0xf
	v_mov_b32_dpp v10, v66 quad_perm:[3,3,3,3] row_mask:0xf bank_mask:0xf
	v_perm_b32 v67, v42, v58, v1
	v_perm_b32 v68, v10, v26, v1
	v_perm_b32 v69, v68, v67, s98
	v_add_u32_e32 v70, 0x8000, v82
	global_store_dword v70, v69, s[2:3]
	v_mul_f32_e32 v59, v59, v75
	v_mul_f32_e32 v43, v43, v75
	v_mul_f32_e32 v27, v27, v75
	v_mul_f32_e32 v11, v11, v75
	v_mul_f32_e32 v59, 0x41800000, v59
	v_mul_f32_e32 v43, 0x41800000, v43
	v_mul_f32_e32 v27, 0x41800000, v27
	v_mul_f32_e32 v11, 0x41800000, v11
	v_med3_f32 v59, v59, s54, v221
	v_med3_f32 v43, v43, s54, v221
	v_med3_f32 v27, v27, s54, v221
	v_med3_f32 v11, v11, s54, v221
	v_cvt_pk_fp8_f32 v71, v59, v43
	v_cvt_pk_fp8_f32 v71, v27, v11 op_sel:[0,0,1]
	s_nop 1
	v_mov_b32_dpp v59, v71 quad_perm:[0,0,0,0] row_mask:0xf bank_mask:0xf
	v_mov_b32_dpp v43, v71 quad_perm:[1,1,1,1] row_mask:0xf bank_mask:0xf
	v_mov_b32_dpp v27, v71 quad_perm:[2,2,2,2] row_mask:0xf bank_mask:0xf
	v_mov_b32_dpp v11, v71 quad_perm:[3,3,3,3] row_mask:0xf bank_mask:0xf
	v_perm_b32 v72, v43, v59, v1
	v_perm_b32 v73, v11, v27, v1
	v_perm_b32 v69, v73, v72, s98
	v_add_u32_e32 v70, 0x8800, v82
	global_store_dword v70, v69, s[2:3]
	v_mul_f32_e32 v60, v60, v76
	v_mul_f32_e32 v44, v44, v76
	v_mul_f32_e32 v28, v28, v76
	v_mul_f32_e32 v12, v12, v76
	v_mul_f32_e32 v60, 0x41800000, v60
	v_mul_f32_e32 v44, 0x41800000, v44
	v_mul_f32_e32 v28, 0x41800000, v28
	v_mul_f32_e32 v12, 0x41800000, v12
	v_med3_f32 v60, v60, s54, v221
	v_med3_f32 v44, v44, s54, v221
	v_med3_f32 v28, v28, s54, v221
	v_med3_f32 v12, v12, s54, v221
	v_cvt_pk_fp8_f32 v66, v60, v44
	v_cvt_pk_fp8_f32 v66, v28, v12 op_sel:[0,0,1]
	s_nop 1
	v_mov_b32_dpp v60, v66 quad_perm:[0,0,0,0] row_mask:0xf bank_mask:0xf
	v_mov_b32_dpp v44, v66 quad_perm:[1,1,1,1] row_mask:0xf bank_mask:0xf
; __device__ __forceinline__ int crow(int r, int hi) { return (r & 3) + 8 * (r >> 2) + 4 * hi; }
; __device__ __forceinline__ void attn_unit(const bf16* __restrict__ Qlane, const bf16* __restrict__ Kh, const bf16* __restrict__ Vh, unsigned char* __restrict__ Ow, int ldo, ...
;     ...
;   for (int r = 0; r < 16; ++r) rli[r] = __builtin_amdgcn_rcpf(li_l[crow(r, hi)]);
;   unsigned ob = (unsigned)(4 * hi * ldo + r32); asm volatile("" : "+v"(ob));
; #pragma unroll
;   for (int r = 0; r < 16; ++r) { const int orow0 = crow(r, 0);
; #pragma unroll
;     for (int d0 = 0; d0 < 4; ++d0) Ow[ob + (unsigned)(orow0 * ldo + d0 * 32)] = (unsigned char)(__builtin_amdgcn_cvt_pk_fp8_f32(__builtin_amdgcn_fmed3f(o[d0][r] * rli[r] * F8_MSCALE, -448.f, 448.f), 0.f, 0, false) & 0xff); }
;   __syncthreads();
; __device__ __forceinline__ void ph5_body(const Args& a, char* ldsg, int wave, int lane, int G, int bid) {
;     ...
;     for (int L = bid; L < NB * NCHUNK * NKVH; L += G) {
	v_mov_b32_dpp v28, v66 quad_perm:[2,2,2,2] row_mask:0xf bank_mask:0xf
	v_mov_b32_dpp v12, v66 quad_perm:[3,3,3,3] row_mask:0xf bank_mask:0xf
	v_perm_b32 v67, v44, v60, v1
	v_perm_b32 v68, v12, v28, v1
	v_perm_b32 v69, v68, v67, s98
	v_add_u32_e32 v70, 0x9000, v82
	global_store_dword v70, v69, s[2:3]
	v_mul_f32_e32 v61, v61, v77
	v_mul_f32_e32 v45, v45, v77
	v_mul_f32_e32 v29, v29, v77
	v_mul_f32_e32 v13, v13, v77
	v_mul_f32_e32 v61, 0x41800000, v61
	v_mul_f32_e32 v45, 0x41800000, v45
	v_mul_f32_e32 v29, 0x41800000, v29
	v_mul_f32_e32 v13, 0x41800000, v13
	v_med3_f32 v61, v61, s54, v221
	v_med3_f32 v45, v45, s54, v221
	v_med3_f32 v29, v29, s54, v221
	v_med3_f32 v13, v13, s54, v221
	v_cvt_pk_fp8_f32 v71, v61, v45
	v_cvt_pk_fp8_f32 v71, v29, v13 op_sel:[0,0,1]
	s_nop 1
	v_mov_b32_dpp v61, v71 quad_perm:[0,0,0,0] row_mask:0xf bank_mask:0xf
	v_mov_b32_dpp v45, v71 quad_perm:[1,1,1,1] row_mask:0xf bank_mask:0xf
	v_mov_b32_dpp v29, v71 quad_perm:[2,2,2,2] row_mask:0xf bank_mask:0xf
	v_mov_b32_dpp v13, v71 quad_perm:[3,3,3,3] row_mask:0xf bank_mask:0xf
	v_perm_b32 v72, v45, v61, v1
	v_perm_b32 v73, v13, v29, v1
	v_perm_b32 v69, v73, v72, s98
	v_add_u32_e32 v70, 0x9800, v82
	global_store_dword v70, v69, s[2:3]
	v_mul_f32_e32 v62, v62, v78
	v_mul_f32_e32 v46, v46, v78
	v_mul_f32_e32 v30, v30, v78
	v_mul_f32_e32 v14, v14, v78
	v_mul_f32_e32 v62, 0x41800000, v62
	v_mul_f32_e32 v46, 0x41800000, v46
	v_mul_f32_e32 v30, 0x41800000, v30
	v_mul_f32_e32 v14, 0x41800000, v14
	v_med3_f32 v62, v62, s54, v221
	v_med3_f32 v46, v46, s54, v221
	v_med3_f32 v30, v30, s54, v221
	v_med3_f32 v14, v14, s54, v221
	v_cvt_pk_fp8_f32 v66, v62, v46
	v_cvt_pk_fp8_f32 v66, v30, v14 op_sel:[0,0,1]
	s_nop 1
	v_mov_b32_dpp v62, v66 quad_perm:[0,0,0,0] row_mask:0xf bank_mask:0xf
	v_mov_b32_dpp v46, v66 quad_perm:[1,1,1,1] row_mask:0xf bank_mask:0xf
	v_mov_b32_dpp v30, v66 quad_perm:[2,2,2,2] row_mask:0xf bank_mask:0xf
	v_mov_b32_dpp v14, v66 quad_perm:[3,3,3,3] row_mask:0xf bank_mask:0xf
	v_perm_b32 v67, v46, v62, v1
	v_perm_b32 v68, v14, v30, v1
	v_perm_b32 v69, v68, v67, s98
	v_add_u32_e32 v70, 0xc000, v82
	global_store_dword v70, v69, s[2:3]
	v_mul_f32_e32 v63, v63, v79
	v_mul_f32_e32 v47, v47, v79
	v_mul_f32_e32 v31, v31, v79
	v_mul_f32_e32 v15, v15, v79
	v_mul_f32_e32 v63, 0x41800000, v63
	v_mul_f32_e32 v47, 0x41800000, v47
	v_mul_f32_e32 v31, 0x41800000, v31
	v_mul_f32_e32 v15, 0x41800000, v15
	v_med3_f32 v63, v63, s54, v221
	v_med3_f32 v47, v47, s54, v221
	v_med3_f32 v31, v31, s54, v221
	v_med3_f32 v15, v15, s54, v221
	v_cvt_pk_fp8_f32 v71, v63, v47
	v_cvt_pk_fp8_f32 v71, v31, v15 op_sel:[0,0,1]
	s_nop 1
	v_mov_b32_dpp v63, v71 quad_perm:[0,0,0,0] row_mask:0xf bank_mask:0xf
	v_mov_b32_dpp v47, v71 quad_perm:[1,1,1,1] row_mask:0xf bank_mask:0xf
	v_mov_b32_dpp v31, v71 quad_perm:[2,2,2,2] row_mask:0xf bank_mask:0xf
	v_mov_b32_dpp v15, v71 quad_perm:[3,3,3,3] row_mask:0xf bank_mask:0xf
	v_perm_b32 v72, v47, v63, v1
	v_perm_b32 v73, v15, v31, v1
	v_perm_b32 v69, v73, v72, s98
	v_add_u32_e32 v70, 0xc800, v82
	global_store_dword v70, v69, s[2:3]
	v_mul_f32_e32 v64, v64, v80
	v_mul_f32_e32 v48, v48, v80
	v_mul_f32_e32 v32, v32, v80
	v_mul_f32_e32 v16, v16, v80
	v_mul_f32_e32 v64, 0x41800000, v64
	v_mul_f32_e32 v48, 0x41800000, v48
	v_mul_f32_e32 v32, 0x41800000, v32
	v_mul_f32_e32 v16, 0x41800000, v16
	v_med3_f32 v64, v64, s54, v221
	v_med3_f32 v48, v48, s54, v221
	v_med3_f32 v32, v32, s54, v221
	v_med3_f32 v16, v16, s54, v221
	v_cvt_pk_fp8_f32 v66, v64, v48
	v_cvt_pk_fp8_f32 v66, v32, v16 op_sel:[0,0,1]
	s_nop 1
	v_mov_b32_dpp v64, v66 quad_perm:[0,0,0,0] row_mask:0xf bank_mask:0xf
	v_mov_b32_dpp v48, v66 quad_perm:[1,1,1,1] row_mask:0xf bank_mask:0xf
	v_mov_b32_dpp v32, v66 quad_perm:[2,2,2,2] row_mask:0xf bank_mask:0xf
	v_mov_b32_dpp v16, v66 quad_perm:[3,3,3,3] row_mask:0xf bank_mask:0xf
	v_perm_b32 v67, v48, v64, v1
	v_perm_b32 v68, v16, v32, v1
	v_perm_b32 v69, v68, v67, s98
	v_add_u32_e32 v70, 0xd000, v82
	global_store_dword v70, v69, s[2:3]
	v_mul_f32_e32 v65, v65, v81
	v_mul_f32_e32 v49, v49, v81
	v_mul_f32_e32 v33, v33, v81
	v_mul_f32_e32 v17, v17, v81
	v_mul_f32_e32 v65, 0x41800000, v65
	v_mul_f32_e32 v49, 0x41800000, v49
	v_mul_f32_e32 v33, 0x41800000, v33
	v_mul_f32_e32 v17, 0x41800000, v17
	v_med3_f32 v65, v65, s54, v221
	v_med3_f32 v49, v49, s54, v221
	v_med3_f32 v33, v33, s54, v221
	v_med3_f32 v17, v17, s54, v221
	v_cvt_pk_fp8_f32 v71, v65, v49
	v_cvt_pk_fp8_f32 v71, v33, v17 op_sel:[0,0,1]
	s_nop 1
	v_mov_b32_dpp v65, v71 quad_perm:[0,0,0,0] row_mask:0xf bank_mask:0xf
	v_mov_b32_dpp v49, v71 quad_perm:[1,1,1,1] row_mask:0xf bank_mask:0xf
	v_mov_b32_dpp v33, v71 quad_perm:[2,2,2,2] row_mask:0xf bank_mask:0xf
	v_mov_b32_dpp v17, v71 quad_perm:[3,3,3,3] row_mask:0xf bank_mask:0xf
	v_perm_b32 v72, v49, v65, v1
	v_perm_b32 v73, v17, v33, v1
	v_perm_b32 v69, v73, v72, s98
	v_add_u32_e32 v70, 0xd800, v82
	global_store_dword v70, v69, s[2:3]
	s_add_i32 s55, s55, s88
	s_add_i32 s47, s47, s48
	s_cmpk_lt_i32 s55, 0x200
	s_waitcnt vmcnt(63) expcnt(7) lgkmcnt(15)
	s_barrier
	s_cbranch_scc0 .LBB0_801
